# weight-conversion schedule: in_proj l0 spare share 60 -> 10 blocks (50 more per layer inside the mixer phases), out_proj l0 485, in_proj l1 475
# speedup vs baseline: 1.0022x; 1.0022x over previous
.LBB0_310:
	s_lshl_b32 s4, s2, 3
	v_writelane_b32 v254, s4, 7
	s_lshl_b32 s4, s3, 3
	v_writelane_b32 v254, s4, 8
	s_lshl_b32 s4, s2, 9
	s_lshl_b32 s62, s3, 9
	s_cmp_eq_u32 s2, 0
	v_writelane_b32 v254, s4, 9
	s_cselect_b64 s[4:5], -1, 0
	v_writelane_b32 v254, s4, 10
	s_lshl_b32 s8, s2, 5
	s_and_b32 s14, s87, 31
	v_writelane_b32 v254, s5, 11
	s_mul_i32 s4, s2, 0x6b
	s_add_i32 s7, s4, 0xffffd954
	s_ashr_i32 s11, s87, 5
	s_lshl_b32 s4, s2, 4
	s_lshl_b32 s66, s3, 4
	s_cmpk_lt_i32 s2, 0x100
	v_writelane_b32 v254, s4, 12
	s_cselect_b64 s[4:5], -1, 0
	v_writelane_b32 v254, s4, 13
	s_movk_i32 s64, 0x80
	s_movk_i32 s65, 0xff00
	v_writelane_b32 v254, s5, 14
	s_lshr_b32 s4, s2, 3
	s_mul_i32 s4, s4, 5
	s_and_b32 s5, s2, 7
	s_add_i32 s4, s4, s5
	s_add_i32 s4, s4, -3
	s_cmp_lt_u32 s5, 3
	s_cselect_b32 s4, 0x7fff, s4
	s_cmpk_lt_i32 s4, 0x80
	v_writelane_b32 v254, s4, 15
	s_cselect_b64 s[4:5], -1, 0
	s_and_b32 s9, s87, 3
	v_writelane_b32 v254, s4, 16
	s_cmpk_lt_i32 s2, 0x200
	s_movk_i32 s56, 0x1000
	v_writelane_b32 v254, s5, 17
	s_cselect_b64 s[4:5], -1, 0
	v_writelane_b32 v254, s4, 18
	s_lshl_b32 s74, s3, 5
	s_movk_i32 s77, 0x4400
	v_writelane_b32 v254, s5, 19
	s_lshl_b32 s4, s2, 2
	s_and_b32 s4, s4, 0xffffff00
	v_writelane_b32 v254, s4, 20
	s_lshl_b32 s4, s2, 6
	s_and_b32 s6, s4, 0xfc0
	s_cmp_gt_i32 s3, 0
	v_writelane_b32 v254, s4, 21
	s_cselect_b64 s[4:5], -1, 0
	v_writelane_b32 v254, s4, 22
	s_ashr_i32 s12, s87, 2
	s_mov_b32 s10, s12
	v_writelane_b32 v254, s5, 23
	s_ashr_i32 s4, s87, 3
	v_writelane_b32 v254, s4, 24
	s_and_b32 s5, s87, 7
	s_lshl_b32 s4, s5, 7
	v_writelane_b32 v254, s5, 25
	s_lshl_b32 s5, s5, 18
	v_writelane_b32 v254, s5, 26
	s_ashr_i32 s13, s12, 31
	v_writelane_b32 v254, s10, 27
	s_lshl_b64 s[12:13], s[12:13], 18
	s_lshl_b32 s5, s9, 8
	v_writelane_b32 v254, s11, 28
	v_writelane_b32 v254, s12, 29
	s_mov_b32 s38, 0x78787879
	s_movk_i32 s39, 0xef00
	v_writelane_b32 v254, s13, 30
	v_writelane_b32 v254, s9, 31
	s_lshl_b32 s9, s9, 18
	s_cmpk_lt_i32 s2, 0x84
	v_writelane_b32 v254, s9, 32
	s_cselect_b32 s9, 32, 0x6b
	v_writelane_b32 v254, s9, 33
	v_writelane_b32 v254, s8, 34
	s_cselect_b32 s7, s8, s7
	v_writelane_b32 v254, s7, 35
	s_add_i32 s7, s3, -1
	s_cmp_gt_u32 s7, 6
	s_cselect_b64 s[8:9], -1, 0
	s_abs_i32 s12, s3
	v_cvt_f32_u32_e32 v1, s12
	v_writelane_b32 v254, s8, 36
	s_sub_i32 s7, 0, s12
	s_and_b32 s76, s3, 0x7ffffff8
	v_rcp_iflag_f32_e32 v1, v1
	v_writelane_b32 v254, s9, 37
	s_ashr_i32 s13, s3, 31
	s_mov_b32 s59, 0x800000
	v_mul_f32_e32 v1, 0x4f7ffffe, v1
	v_cvt_u32_f32_e32 v1, v1
	v_mov_b32_e32 v205, 1
	v_mov_b32_e32 v221, 0x1400
	v_mov_b32_e32 v204, 0x20200
	v_readfirstlane_b32 s8, v1
	s_mul_i32 s7, s7, s8
	s_mul_hi_u32 s7, s8, s7
	s_add_i32 s7, s8, s7
	v_writelane_b32 v254, s7, 38
	s_mul_hi_u32 s7, s7, 0xa1b
	s_mul_i32 s8, s7, s12
	s_sub_i32 s8, 0xa1b, s8
	s_add_i32 s9, s7, 1
	s_sub_i32 s10, s8, s12
	s_cmp_ge_u32 s8, s12
	s_cselect_b32 s7, s9, s7
	s_cselect_b32 s8, s10, s8
	s_add_i32 s9, s7, 1
	s_cmp_ge_u32 s8, s12
	s_cselect_b32 s7, s9, s7
	s_xor_b32 s7, s7, s13
	s_sub_i32 s7, s7, s13
	s_mul_i32 s8, s7, s3
	s_sub_i32 s8, 0xa1b, s8
	s_mul_i32 s9, s7, s87
	s_min_i32 s10, s87, s8
	v_writelane_b32 v254, s12, 39
	s_add_i32 s9, s9, s10
	v_writelane_b32 v254, s13, 40
	s_cmp_lt_i32 s87, s8
	v_writelane_b32 v254, s9, 41
	s_cselect_b64 s[8:9], -1, 0
	s_cmp_lg_u64 s[8:9], 0
	s_addc_u32 s7, s7, 0
	v_writelane_b32 v254, s7, 42
	s_lshl_b32 s7, s3, 1
	v_writelane_b32 v254, s7, 43
	s_add_i32 s7, s11, 17
	v_writelane_b32 v254, s7, 44
	s_lshl_b32 s7, s7, 4
	v_writelane_b32 v254, s7, 45
	s_lshl_b32 s7, s14, 4
	v_writelane_b32 v254, s14, 46
	s_add_i32 s8, s7, 0xbea0
	v_writelane_b32 v254, s8, 47
	s_add_i32 s8, s11, 9
	v_writelane_b32 v254, s8, 48
	s_lshl_b32 s8, s8, 4
	v_writelane_b32 v254, s8, 49
	v_writelane_b32 v254, s11, 50
	s_add_i32 s8, s11, 1
	v_writelane_b32 v254, s8, 51
	s_or_b32 s8, s7, 0xfffffe00
	v_writelane_b32 v254, s8, 52
	s_lshl_b32 s8, s3, 6
	v_writelane_b32 v254, s8, 53
	s_add_i32 s7, s7, 0xa050
	v_writelane_b32 v254, s7, 54
	s_add_i32 s7, 0, 0x12000
	v_writelane_b32 v254, s7, 55
	s_add_i32 s7, 0, 0x27020
	v_writelane_b32 v254, s7, 56
	s_add_i32 s7, 0, 0x27024
	v_writelane_b32 v254, s7, 57
	s_add_i32 s7, 0, 0x25000
	v_writelane_b32 v254, s7, 58
	s_lshl_b32 s6, s6, 1
	v_writelane_b32 v254, s6, 59
	s_lshl_b32 s5, s5, 2
	v_writelane_b32 v254, s5, 60
	s_add_i32 s5, 0, 0x25400
	v_writelane_b32 v254, s5, 61
	s_add_i32 s5, 0, 0x10200
	v_writelane_b32 v254, s5, 62
	s_add_i32 s5, 0, 0x20100
	v_writelane_b32 v254, s5, 63
	s_add_i32 s5, 0, 0x20010
	v_writelane_b32 v255, s5, 0
	s_add_i32 s5, 0, 0x20110
	v_writelane_b32 v255, s5, 1
	s_add_i32 s5, 0, 0x20020
	v_writelane_b32 v255, s5, 2
	s_add_i32 s5, 0, 0x20120
	v_writelane_b32 v255, s5, 3
	s_add_i32 s5, 0, 0x20030
	v_writelane_b32 v255, s5, 4
	s_add_i32 s5, 0, 0x20130
	v_writelane_b32 v255, s5, 5
	s_add_i32 s5, 0, 0x20040
	v_writelane_b32 v255, s5, 6
	s_add_i32 s5, 0, 0x20140
	v_writelane_b32 v255, s5, 7
	s_add_i32 s5, 0, 0x20050
	v_writelane_b32 v255, s5, 8
	s_add_i32 s5, 0, 0x20150
	v_writelane_b32 v255, s5, 9
	s_add_i32 s5, 0, 0x20060
	v_writelane_b32 v255, s5, 10
	s_add_i32 s5, 0, 0x20160
	v_writelane_b32 v255, s5, 11
	s_add_i32 s5, 0, 0x20070
	v_writelane_b32 v255, s5, 12
	s_add_i32 s5, 0, 0x20170
	v_writelane_b32 v255, s5, 13
	s_add_i32 s5, 0, 0x20180
	v_writelane_b32 v255, s5, 14
	s_add_i32 s5, 0, 0x20084
	v_writelane_b32 v255, s5, 15
	s_add_i32 s5, 0, 0x20024
	v_writelane_b32 v255, s5, 16
	s_add_i32 s5, 0, 0x2002c
	v_writelane_b32 v255, s5, 17
	s_add_i32 s5, 0, 0x20034
	v_writelane_b32 v255, s5, 18
	s_add_i32 s5, 0, 0x2003c
	v_writelane_b32 v255, s5, 19
	s_add_i32 s5, 0, 0x20044
	v_writelane_b32 v255, s5, 20
	s_add_i32 s5, 0, 0x2004c
	v_writelane_b32 v255, s5, 21
	s_add_i32 s5, 0, 0x20054
	v_writelane_b32 v255, s5, 22
	s_add_i32 s5, 0, 0x2005c
	v_writelane_b32 v255, s5, 23
	s_add_i32 s5, 0, 0x20064
	v_writelane_b32 v255, s5, 24
	s_add_i32 s5, 0, 0x2006c
	v_writelane_b32 v255, s5, 25
	s_add_i32 s5, 0, 0x20074
	v_writelane_b32 v255, s5, 26
	s_add_i32 s5, 0, 0x2007c
	v_writelane_b32 v255, s5, 27
	s_add_i32 s5, 0, 0x20800
	v_writelane_b32 v255, s5, 28
	s_lshl_b32 s4, s4, 2
	v_writelane_b32 v255, s4, 29
	s_ashr_i32 s63, s62, 31
	s_ashr_i32 s67, s66, 31
	v_writelane_b32 v255, s5, 30
	v_cmp_eq_u32_e64 s[4:5], 0, v0
	s_mov_b32 s6, s74
	s_add_i32 s84, 0, 0x20004
	v_writelane_b32 v255, s4, 31
	s_add_i32 s69, 0, 0x2000c
	s_add_i32 s68, 0, 0x20014
	v_writelane_b32 v255, s5, 32
	s_lshl_b64 s[4:5], s[62:63], 2
	v_writelane_b32 v255, s4, 33
	s_add_i32 s49, 0, 0x2001c
	v_mov_b32_e32 v1, 0
	v_writelane_b32 v255, s5, 34
	s_lshl_b64 s[4:5], s[66:67], 12
	v_writelane_b32 v255, s4, 35
	v_mov_b32_e32 v220, 0xff800000
	s_movk_i32 s47, 0x3ff
	v_writelane_b32 v255, s5, 36
	v_writelane_b32 v255, s6, 37
	s_mov_b32 s83, 0x34400000
	s_mov_b32 s80, 0x36500000
	v_writelane_b32 v255, s7, 38
	s_mov_b32 s6, s62
	v_writelane_b32 v255, s6, 39
	s_movk_i32 s81, 0x7fff
	s_mov_b32 s57, 0x41000000
	v_writelane_b32 v255, s7, 40
	s_mov_b32 s6, s66
	v_writelane_b32 v255, s6, 41
	s_movk_i32 s33, 0xfefe
	s_mov_b32 s85, 0x900000
	v_writelane_b32 v255, s7, 42
	v_writelane_b32 v255, s76, 43
	v_writelane_b32 v255, s84, 44
	s_mov_b32 s72, 0xc0e00000
	s_mov_b32 s73, 0
	s_mov_b32 s71, 0
	s_mov_b64 s[4:5], -1
	s_mov_b64 s[78:79], 0x80
	s_mov_b32 s82, 0x3e38aa3b
	s_mov_b32 s88, 0xc01d265f
	s_mov_b32 s50, s69
	s_mov_b32 s86, s68
	s_mov_b32 s60, s49
	v_writelane_b32 v255, s87, 45
	s_branch .LBB0_314

.LBB0_561:
	s_and_b64 vcc, exec, s[16:17]
	s_cbranch_vccz .LBB0_711
	v_readlane_b32 s6, v254, 50
	v_readlane_b32 s7, v254, 46
	s_mul_i32 s6, s35, s6
	s_sub_i32 s7, s7, s36
	s_add_i32 s23, s7, s6
	s_lshl_b32 s22, s35, 3
	s_mov_b64 s[6:7], -1
	s_and_b64 vcc, exec, s[90:91]
	s_cbranch_vccz .LBB0_637
	v_mbcnt_lo_u32_b32 v66, -1, 0
	v_mbcnt_hi_u32_b32 v66, -1, v66
	s_getreg_b32 s6, hwreg(HW_REG_HW_ID, 0, 6)
	s_lshl_b32 s6, s6, 2
	s_and_b32 s6, s6, 0xfc
	s_or_b32 s6, s6, 0x27100
	v_mov_b32_e32 v0, s6
	ds_read_b32 v0, v0
	s_cmpk_gt_i32 s23, 0x1da
	s_waitcnt lgkmcnt(0)
	v_readfirstlane_b32 s9, v0
	s_cbranch_scc1 .LBB0_636
	s_add_i32 s20, s23, 0xc0a
	s_mul_hi_i32 s6, s20, 0x2aaaaaab
	s_lshr_b32 s7, s6, 31
	s_ashr_i32 s15, s6, 9
	s_add_i32 s15, s15, s7
	s_mul_i32 s16, s15, 0xfffff400
	s_add_i32 s16, s16, s20
	s_cmpk_gt_i32 s16, 0x7ff
	s_mov_b64 s[12:13], -1
	s_cbranch_scc0 .LBB0_566
	s_add_i32 s6, s16, 0xfffff800
	s_mov_b32 s10, 31
	s_lshl_b32 s7, s15, 5
	s_lshr_b32 s6, s6, 5
	s_lshl_b32 s24, s20, 8
	s_ashr_i32 s11, s10, 31
	s_add_i32 s6, s6, s7
	s_lshl_b32 s14, s20, 5
	s_and_b32 s8, s24, 0x300
	s_lshl_b64 s[10:11], s[10:11], 3
	s_add_u32 s10, s0, s10
	s_addc_u32 s11, s1, s11
	s_load_dwordx2 s[10:11], s[10:11], 0x0
	s_ashr_i32 s7, s6, 31
	s_lshl_b64 s[12:13], s[6:7], 20
	s_lshl_b64 s[6:7], s[6:7], 22
	s_waitcnt lgkmcnt(0)
	s_add_u32 s6, s10, s6
	s_mov_b32 s10, 35
	s_addc_u32 s7, s11, s7
	s_ashr_i32 s11, s10, 31
	s_lshl_b64 s[10:11], s[10:11], 3
	s_add_u32 s10, s0, s10
	s_addc_u32 s11, s1, s11
	s_load_dwordx2 s[10:11], s[10:11], 0x0
	s_waitcnt lgkmcnt(0)
	s_add_u32 s10, s10, s12
	s_addc_u32 s11, s11, s13
	s_add_u32 s10, s10, 0x12800000
	s_addc_u32 s11, s11, 0
	s_mov_b64 s[12:13], 0

.LBB0_569:
	v_lshl_or_b32 v67, s9, 6, v66
	v_ashrrev_i32_e32 v69, 6, v67
	s_and_b32 s14, s14, 0x380
	v_lshlrev_b32_e32 v135, 4, v69
	v_add_u32_e32 v0, s14, v135
	s_waitcnt vmcnt(0)
	v_mad_i64_i32 v[2:3], s[16:17], s12, v0, 0
	v_and_b32_e32 v68, 63, v66
	v_lshl_add_u64 v[2:3], v[2:3], 2, s[6:7]
	s_mov_b32 s9, s71
	v_lshl_add_u64 v[2:3], s[8:9], 2, v[2:3]
	v_lshlrev_b32_e32 v0, 4, v68
	v_lshl_add_u64 v[2:3], v[2:3], 0, v[0:1]
	s_lshl_b32 s70, s12, 2
	v_lshl_add_u64 v[10:11], v[2:3], 0, s[70:71]
	global_load_dwordx4 v[2:5], v[2:3], off nt
	s_nop 0
	global_load_dwordx4 v[6:9], v[10:11], off nt
	v_lshl_add_u64 v[10:11], v[10:11], 0, s[70:71]
	v_lshl_add_u64 v[18:19], v[10:11], 0, s[70:71]
	global_load_dwordx4 v[10:13], v[10:11], off nt
	s_nop 0
	global_load_dwordx4 v[14:17], v[18:19], off nt
	v_lshl_add_u64 v[18:19], v[18:19], 0, s[70:71]
	v_lshl_add_u64 v[26:27], v[18:19], 0, s[70:71]
	global_load_dwordx4 v[18:21], v[18:19], off nt
	s_nop 0
	global_load_dwordx4 v[22:25], v[26:27], off nt
	v_lshl_add_u64 v[26:27], v[26:27], 0, s[70:71]
	v_lshl_add_u64 v[34:35], v[26:27], 0, s[70:71]
	v_lshl_add_u64 v[38:39], v[34:35], 0, s[70:71]
	v_lshl_add_u64 v[42:43], v[38:39], 0, s[70:71]
	v_lshl_add_u64 v[46:47], v[42:43], 0, s[70:71]
	v_lshl_add_u64 v[50:51], v[46:47], 0, s[70:71]
	v_lshl_add_u64 v[54:55], v[50:51], 0, s[70:71]
	v_lshl_add_u64 v[58:59], v[54:55], 0, s[70:71]
	v_lshl_add_u64 v[62:63], v[58:59], 0, s[70:71]
	global_load_dwordx4 v[26:29], v[26:27], off nt
	s_nop 0
	global_load_dwordx4 v[30:33], v[34:35], off nt
	v_lshlrev_b32_e32 v134, 2, v68
	global_load_dwordx4 v[34:37], v[38:39], off nt
	v_lshl_add_u32 v0, v68, 9, 0
	global_load_dwordx4 v[38:41], v[42:43], off nt
	v_bitop3_b32 v68, v69, v66, 7 bitop3:0x78
	global_load_dwordx4 v[42:45], v[46:47], off nt
	v_lshrrev_b32_e32 v69, 5, v67
	global_load_dwordx4 v[46:49], v[50:51], off nt
	v_xor_b32_e32 v69, v69, v66
	global_load_dwordx4 v[50:53], v[54:55], off nt
	v_readlane_b32 s6, v254, 44
	global_load_dwordx4 v[54:57], v[58:59], off nt
	v_lshlrev_b32_e32 v69, 4, v69
	global_load_dwordx4 v[58:61], v[62:63], off nt
	v_lshl_add_u64 v[62:63], v[62:63], 0, s[70:71]
	global_load_dwordx4 v[62:65], v[62:63], off nt
	v_ashrrev_i32_e32 v140, 3, v67
	v_add_u32_e32 v70, 0x200, v67
	v_add_u32_e32 v71, 0x400, v67
	v_add_u32_e32 v67, 0x600, v67
	s_mul_i32 s26, s6, s35
	v_readlane_b32 s6, v254, 48
	v_and_b32_e32 v69, 0x70, v69
	v_lshlrev_b32_e32 v66, 4, v66
	v_ashrrev_i32_e32 v141, 3, v70
	v_ashrrev_i32_e32 v142, 3, v71
	v_ashrrev_i32_e32 v143, 3, v67
	s_mul_i32 s29, s6, s35
	v_readlane_b32 s6, v254, 51
	v_lshlrev_b32_e32 v68, 4, v68
	v_add_u32_e32 v69, 0, v69
	v_and_b32_e32 v136, 0x70, v66
	v_lshlrev_b32_e32 v66, 7, v140
	v_lshlrev_b32_e32 v70, 7, v141
	v_lshlrev_b32_e32 v71, 7, v142
	v_lshlrev_b32_e32 v67, 7, v143
	s_mul_i32 s6, s6, s35
	v_mov_b32_e32 v137, v1
	s_lshl_b32 s25, s35, 12
	s_lshl_b32 s27, s35, 4
	s_lshl_b32 s28, s35, 8
	s_add_i32 s30, s6, 0xbea
	v_add_u32_e32 v144, v0, v68
	v_add_u32_e32 v145, v69, v66
	v_add_u32_e32 v146, v69, v70
	v_add_u32_e32 v147, v69, v71
	v_add_u32_e32 v148, v69, v67
	v_readlane_b32 s36, v254, 47
	s_mov_b32 s70, s14
	s_mov_b32 s37, s31
	s_mov_b32 s12, s8
	s_mov_b64 s[16:17], s[10:11]
	s_branch .LBB0_573

.LBB0_573:
	v_readlane_b32 s6, v254, 46
	s_add_i32 s6, s6, s29
	s_add_i32 s9, s20, s22
	s_add_i32 s7, s6, 0xbea
	s_cmpk_lt_i32 s7, 0xde5
	s_cselect_b64 s[18:19], -1, 0
	s_cmpk_gt_i32 s7, 0xde4
	s_cbranch_scc1 .LBB0_580
	s_mul_hi_i32 s7, s7, 0x2aaaaaab
	s_lshr_b32 s12, s7, 31
	s_ashr_i32 s20, s7, 9
	s_add_i32 s20, s20, s12
	s_mul_i32 s7, s20, 0xfffff400
	s_add_i32 s37, s6, s7
	s_add_i32 s21, s37, 0xbea
	s_cmpk_gt_i32 s21, 0x7ff
	s_mov_b64 s[14:15], -1
	s_cbranch_scc0 .LBB0_576
	s_addk_i32 s37, 0x3ea
	s_mov_b32 s14, 31
	s_lshl_b32 s6, s20, 5
	s_lshr_b32 s7, s37, 5
	s_ashr_i32 s15, s14, 31
	s_add_i32 s6, s7, s6
	s_lshl_b32 s13, s9, 5
	s_and_b32 s12, s24, 0x300
	s_lshl_b64 s[14:15], s[14:15], 3
	s_add_u32 s14, s0, s14
	s_addc_u32 s15, s1, s15
	s_load_dwordx2 s[14:15], s[14:15], 0x0
	s_ashr_i32 s7, s6, 31
	s_lshl_b64 s[16:17], s[6:7], 20
	s_lshl_b64 s[6:7], s[6:7], 22
	s_waitcnt lgkmcnt(0)
	s_add_u32 s6, s14, s6
	s_mov_b32 s14, 35
	s_addc_u32 s7, s15, s7
	s_ashr_i32 s15, s14, 31
	s_lshl_b64 s[14:15], s[14:15], 3
	s_add_u32 s14, s0, s14
	s_addc_u32 s15, s1, s15
	s_load_dwordx2 s[14:15], s[14:15], 0x0
	s_waitcnt lgkmcnt(0)
	s_add_u32 s14, s14, s16
	s_addc_u32 s15, s15, s17
	s_add_u32 s16, s14, 0x12800000
	s_addc_u32 s17, s15, 0
	s_mov_b64 s[14:15], 0

.LBB0_604:
	v_ashrrev_i32_e32 v139, 31, v138
	v_lshlrev_b64 v[138:139], 10, v[138:139]
	v_lshl_add_u64 v[138:139], s[10:11], 0, v[138:139]
	v_lshl_add_u64 v[138:139], v[138:139], 0, s[70:71]
	v_lshl_add_u64 v[138:139], v[138:139], 0, v[136:137]
	s_andn2_b64 vcc, exec, s[18:19]
	s_mov_b64 s[6:7], -1
	s_waitcnt lgkmcnt(0)
	global_store_dwordx4 v[138:139], v[130:133], off nt
	s_cbranch_vccnz .LBB0_572
	v_readlane_b32 s6, v254, 46
	s_add_i32 s6, s6, s26
	s_add_i32 s20, s9, s22
	s_add_i32 s7, s6, 0xbea
	s_cmpk_gt_i32 s7, 0xde4
	s_cbranch_scc1 .LBB0_612
	s_mul_hi_i32 s7, s7, 0x2aaaaaab
	s_lshr_b32 s8, s7, 31
	s_ashr_i32 s13, s7, 9
	s_add_i32 s13, s13, s8
	s_mul_i32 s7, s13, 0xfffff400
	s_add_i32 s21, s6, s7
	s_add_i32 s15, s21, 0xbea
	s_cmpk_gt_i32 s15, 0x7ff
	s_mov_b64 s[18:19], -1
	s_cbranch_scc0 .LBB0_608
	s_addk_i32 s21, 0x525
	s_mov_b32 s10, 31
	s_lshl_b32 s6, s13, 5
	s_lshr_b32 s7, s21, 5
	s_ashr_i32 s11, s10, 31
	s_add_i32 s6, s7, s6
	s_lshl_b32 s9, s20, 5
	s_and_b32 s8, s24, 0x300
	s_lshl_b64 s[10:11], s[10:11], 3
	s_add_u32 s10, s0, s10
	s_addc_u32 s11, s1, s11
	s_load_dwordx2 s[10:11], s[10:11], 0x0
	s_ashr_i32 s7, s6, 31
	s_lshl_b64 s[18:19], s[6:7], 20
	s_lshl_b64 s[6:7], s[6:7], 22
	s_waitcnt lgkmcnt(0)
	s_add_u32 s6, s10, s6
	s_mov_b32 s10, 35
	s_addc_u32 s7, s11, s7
	s_ashr_i32 s11, s10, 31
	s_lshl_b64 s[10:11], s[10:11], 3
	s_add_u32 s10, s0, s10
	s_addc_u32 s11, s1, s11
	s_load_dwordx2 s[10:11], s[10:11], 0x0
	s_waitcnt lgkmcnt(0)
	s_add_u32 s10, s10, s18
	s_addc_u32 s11, s11, s19
	s_add_u32 s10, s10, 0x12800000
	s_addc_u32 s11, s11, 0
	s_mov_b64 s[18:19], 0

.LBB0_1405:
	s_andn2_b64 vcc, exec, s[6:7]
	s_cbranch_vccnz .LBB0_1479
	v_mbcnt_lo_u32_b32 v66, -1, 0
	v_mbcnt_hi_u32_b32 v66, -1, v66
	s_getreg_b32 s6, hwreg(HW_REG_HW_ID, 0, 6)
	s_lshl_b32 s6, s6, 2
	s_and_b32 s6, s6, 0xfc
	s_or_b32 s6, s6, 0x27100
	v_mov_b32_e32 v0, s6
	ds_read_b32 v0, v0
	v_readlane_b32 s6, v254, 50
	v_readlane_b32 s7, v254, 46
	s_mul_i32 s6, s37, s6
	s_sub_i32 s7, s7, s40
	s_add_i32 s6, s7, s6
	s_cmpk_gt_i32 s6, 0x1e4
	s_waitcnt lgkmcnt(0)
	v_readfirstlane_b32 s9, v0
	s_cbranch_scc1 .LBB0_1479
	s_add_i32 s20, s6, 0xa25
	s_mul_hi_i32 s6, s20, 0x2aaaaaab
	s_lshr_b32 s7, s6, 31
	s_ashr_i32 s15, s6, 9
	s_add_i32 s15, s15, s7
	s_mul_i32 s16, s15, 0xfffff400
	s_add_i32 s16, s16, s20
	s_cmpk_gt_i32 s16, 0x7ff
	s_mov_b64 s[12:13], -1
	s_cbranch_scc0 .LBB0_1409
	s_add_i32 s6, s16, 0xfffff800
	s_mov_b32 s10, 31
	s_lshl_b32 s7, s15, 5
	s_lshr_b32 s6, s6, 5
	s_lshl_b32 s22, s20, 8
	s_ashr_i32 s11, s10, 31
	s_add_i32 s6, s6, s7
	s_lshl_b32 s14, s20, 5
	s_and_b32 s8, s22, 0x300
	s_lshl_b64 s[10:11], s[10:11], 3
	s_add_u32 s10, s0, s10
	s_addc_u32 s11, s1, s11
	s_load_dwordx2 s[10:11], s[10:11], 0x0
	s_ashr_i32 s7, s6, 31
	s_lshl_b64 s[12:13], s[6:7], 20
	s_lshl_b64 s[6:7], s[6:7], 22
	s_waitcnt lgkmcnt(0)
	s_add_u32 s6, s10, s6
	s_mov_b32 s10, 35
	s_addc_u32 s7, s11, s7
	s_ashr_i32 s11, s10, 31
	s_lshl_b64 s[10:11], s[10:11], 3
	s_add_u32 s10, s0, s10
	s_addc_u32 s11, s1, s11
	s_load_dwordx2 s[10:11], s[10:11], 0x0
	s_waitcnt lgkmcnt(0)
	s_add_u32 s10, s10, s12
	s_addc_u32 s11, s11, s13
	s_add_u32 s10, s10, 0x12800000
	s_addc_u32 s11, s11, 0
	s_mov_b64 s[12:13], 0

.LBB0_1414:
	v_ashrrev_i32_e32 v139, 31, v138
	v_lshlrev_b64 v[138:139], 10, v[138:139]
	s_add_i32 s31, s31, s26
	v_readlane_b32 s6, v254, 46
	v_lshl_add_u64 v[138:139], s[16:17], 0, v[138:139]
	s_add_i32 s22, s22, s24
	s_add_i32 s25, s25, s26
	s_add_i32 s35, s35, s28
	s_add_i32 s29, s29, s26
	s_add_i32 s6, s6, s31
	v_lshl_add_u64 v[138:139], v[138:139], 0, s[14:15]
	s_cmpk_gt_i32 s6, 0xc09
	v_lshl_add_u64 v[138:139], v[138:139], 0, v[136:137]
	s_cselect_b64 s[6:7], -1, 0
	s_waitcnt lgkmcnt(0)
	global_store_dwordx4 v[138:139], v[130:133], off nt

.LBB0_1416:
	v_readlane_b32 s6, v254, 46
	s_add_i32 s6, s6, s29
	s_add_i32 s9, s20, s23
	s_add_i32 s7, s6, 0xa05
	s_cmpk_lt_i32 s7, 0xc0a
	s_cselect_b64 s[18:19], -1, 0
	s_cmpk_gt_i32 s7, 0xc09
	s_cbranch_scc1 .LBB0_1423
	s_mul_hi_i32 s7, s7, 0x2aaaaaab
	s_lshr_b32 s12, s7, 31
	s_ashr_i32 s20, s7, 9
	s_add_i32 s20, s20, s12
	s_mul_i32 s7, s20, 0xfffff400
	s_add_i32 s37, s6, s7
	s_add_i32 s21, s37, 0xa05
	s_cmpk_gt_i32 s21, 0x7ff
	s_mov_b64 s[14:15], -1
	s_cbranch_scc0 .LBB0_1419
	s_addk_i32 s37, 0x205
	s_mov_b32 s14, 31
	s_lshl_b32 s6, s20, 5
	s_lshr_b32 s7, s37, 5
	s_ashr_i32 s15, s14, 31
	s_add_i32 s6, s7, s6
	s_lshl_b32 s13, s9, 5
	s_and_b32 s12, s22, 0x300
	s_lshl_b64 s[14:15], s[14:15], 3
	s_add_u32 s14, s0, s14
	s_addc_u32 s15, s1, s15
	s_load_dwordx2 s[14:15], s[14:15], 0x0
	s_ashr_i32 s7, s6, 31
	s_lshl_b64 s[16:17], s[6:7], 20
	s_lshl_b64 s[6:7], s[6:7], 22
	s_waitcnt lgkmcnt(0)
	s_add_u32 s6, s14, s6
	s_mov_b32 s14, 35
	s_addc_u32 s7, s15, s7
	s_ashr_i32 s15, s14, 31
	s_lshl_b64 s[14:15], s[14:15], 3
	s_add_u32 s14, s0, s14
	s_addc_u32 s15, s1, s15
	s_load_dwordx2 s[14:15], s[14:15], 0x0
	s_waitcnt lgkmcnt(0)
	s_add_u32 s14, s14, s16
	s_addc_u32 s15, s15, s17
	s_add_u32 s16, s14, 0x12800000
	s_addc_u32 s17, s15, 0
	s_mov_b64 s[14:15], 0

.LBB0_1447:
	v_ashrrev_i32_e32 v139, 31, v138
	v_lshlrev_b64 v[138:139], 10, v[138:139]
	v_lshl_add_u64 v[138:139], s[10:11], 0, v[138:139]
	v_lshl_add_u64 v[138:139], v[138:139], 0, s[70:71]
	v_lshl_add_u64 v[138:139], v[138:139], 0, v[136:137]
	s_andn2_b64 vcc, exec, s[18:19]
	s_mov_b64 s[6:7], -1
	s_waitcnt lgkmcnt(0)
	global_store_dwordx4 v[138:139], v[130:133], off nt
	s_cbranch_vccnz .LBB0_1415
	v_readlane_b32 s6, v254, 46
	s_add_i32 s6, s6, s25
	s_add_i32 s20, s9, s23
	s_add_i32 s7, s6, 0xa05
	s_cmpk_gt_i32 s7, 0xc09
	s_cbranch_scc1 .LBB0_1455
	s_mul_hi_i32 s7, s7, 0x2aaaaaab
	s_lshr_b32 s8, s7, 31
	s_ashr_i32 s13, s7, 9
	s_add_i32 s13, s13, s8
	s_mul_i32 s7, s13, 0xfffff400
	s_add_i32 s21, s6, s7
	s_add_i32 s15, s21, 0xa05
	s_cmpk_gt_i32 s15, 0x7ff
	s_mov_b64 s[18:19], -1
	s_cbranch_scc0 .LBB0_1451
	s_addk_i32 s21, 0x205
	s_mov_b32 s10, 31
	s_lshl_b32 s6, s13, 5
	s_lshr_b32 s7, s21, 5
	s_ashr_i32 s11, s10, 31
	s_add_i32 s6, s7, s6
	s_lshl_b32 s9, s20, 5
	s_and_b32 s8, s22, 0x300
	s_lshl_b64 s[10:11], s[10:11], 3
	s_add_u32 s10, s0, s10
	s_addc_u32 s11, s1, s11
	s_load_dwordx2 s[10:11], s[10:11], 0x0
	s_ashr_i32 s7, s6, 31
	s_lshl_b64 s[18:19], s[6:7], 20
	s_lshl_b64 s[6:7], s[6:7], 22
	s_waitcnt lgkmcnt(0)
	s_add_u32 s6, s10, s6
	s_mov_b32 s10, 35
	s_addc_u32 s7, s11, s7
	s_ashr_i32 s11, s10, 31
	s_lshl_b64 s[10:11], s[10:11], 3
	s_add_u32 s10, s0, s10
	s_addc_u32 s11, s1, s11
	s_load_dwordx2 s[10:11], s[10:11], 0x0
	s_waitcnt lgkmcnt(0)
	s_add_u32 s10, s10, s18
	s_addc_u32 s11, s11, s19
	s_add_u32 s10, s10, 0x12800000
	s_addc_u32 s11, s11, 0
	s_mov_b64 s[18:19], 0
